# speedup vs baseline: 1.0025x; 1.0025x over previous
.LBB0_64:
	s_endpgm
	s_nop 0
	s_nop 0
	s_nop 0
	s_nop 0
	s_nop 0
	s_nop 0
	s_nop 0
	s_nop 0
	s_nop 0
	s_nop 0
	s_nop 0
	s_nop 0
	s_nop 0
	s_nop 0
	s_nop 0
	s_nop 0
	s_nop 0
	s_nop 0
	s_nop 0
	s_nop 0
	s_nop 0
	s_nop 0
	s_nop 0
	s_nop 0
	s_nop 0
	s_nop 0
	s_nop 0
	s_nop 0
	s_nop 0
	s_nop 0
	s_nop 0
	s_nop 0
	s_nop 0
	s_nop 0
	s_nop 0
	s_nop 0
	s_nop 0
	s_endpgm

.LBB1_32:
	s_endpgm
	s_nop 0
	s_nop 0
	s_nop 0
	s_nop 0
	s_nop 0
	s_nop 0
	s_nop 0
	s_nop 0
	s_nop 0
	s_nop 0
	s_nop 0
	s_nop 0
	s_nop 0
	s_nop 0
	s_nop 0
	s_nop 0
	s_nop 0
	s_nop 0
	s_endpgm

.LBB2_29:
	s_or_b64 exec, exec, s[4:5]
	v_or_b32_e32 v14, 16, v69
	v_cmp_lt_i32_e64 s[4:5], v14, v35
	v_mov_b32_e32 v2, v34
	v_mov_b32_e32 v4, 0
	s_and_saveexec_b64 s[6:7], s[4:5]
	s_cbranch_execz .LBB2_31
	v_add_u32_e32 v2, v36, v14
	v_ashrrev_i32_e32 v3, 31, v2
	v_lshl_add_u64 v[2:3], v[2:3], 4, s[30:31]
	global_load_dwordx4 v[2:5], v[2:3], off nt

.LBB2_33:
	s_or_b64 exec, exec, s[8:9]
	s_waitcnt vmcnt(0)
	v_or_b32_e32 v9, 16, v69
	v_lshlrev_b32_e32 v14, 2, v6
	v_lshl_add_u64 v[38:39], v[14:15], 2, s[28:29]
	v_lshlrev_b32_e32 v14, 2, v2
	v_lshl_add_u64 v[16:17], v[14:15], 2, s[28:29]
	v_lshlrev_b32_e32 v14, 2, v10
	v_lshl_add_u64 v[14:15], v[14:15], 2, s[28:29]
	global_load_dwordx3 v[30:32], v[38:39], off offset:4
	global_load_dwordx4 v[22:25], v[16:17], off
	global_load_dwordx4 v[26:29], v[14:15], off
	v_lshlrev_b32_e32 v14, 2, v34
	v_ashrrev_i32_e32 v15, 31, v14
	v_lshlrev_b64 v[14:15], 2, v[14:15]
	s_waitcnt lgkmcnt(0)
	v_lshl_add_u64 v[16:17], s[34:35], 0, v[14:15]
	v_lshl_add_u64 v[14:15], s[28:29], 0, v[14:15]
	global_load_dwordx4 v[18:21], v[16:17], off
	v_cvt_f32_f16_e32 v37, v7
	global_load_dwordx4 v[14:17], v[14:15], off
	v_mov_b32_e32 v5, 0xff800000
	v_mov_b32_e32 v13, 0xff800000
	s_and_saveexec_b64 s[8:9], s[2:3]
	s_cbranch_execz .LBB2_35
	global_load_dword v13, v[38:39], off
	s_waitcnt vmcnt(0)
	v_add_f32_e32 v13, v18, v13
	v_add_f32_e32 v13, v13, v37
	v_mul_f32_e32 v38, 0x3e4ccccd, v13
	v_cmp_lt_f32_e32 vcc, 0, v13
	s_nop 1
	v_cndmask_b32_e32 v13, v38, v13, vcc

.LBB2_38:
	s_cbranch_execz .LBB2_48
	v_mov_b32_e32 v3, 0
	v_mov_b32_e32 v6, v34
	v_mov_b32_e32 v7, 0
	v_mov_b32_e32 v8, 0
	v_mov_b32_e32 v2, v34
	v_mov_b32_e32 v4, 0
	v_or_b32_e32 v10, 16, v69
	v_add_u32_e32 v12, v36, v69
	v_cmp_lt_i32_e64 s[4:5], v10, v35
	v_ashrrev_i32_e32 v13, 31, v12
	v_lshl_add_u64 v[12:13], v[12:13], 4, s[30:31]
	s_mov_b64 s[6:7], exec
	s_mov_b64 exec, s[2:3]
	s_cbranch_execz .Ll1_r2a
	global_load_dwordx4 v[6:9], v[12:13], off nt
.Ll1_r2a:
	s_mov_b64 exec, s[4:5]
	s_cbranch_execz .Ll1_r2b
	global_load_dwordx4 v[2:5], v[12:13], off offset:256 nt
.Ll1_r2b:
	s_mov_b64 exec, s[6:7]
	v_mov_b32_e32 v11, 0
	s_waitcnt vmcnt(0)
	v_or_b32_e32 v9, 16, v69
	v_lshlrev_b32_e32 v10, 2, v6
	v_lshl_add_u64 v[26:27], v[10:11], 2, s[28:29]
	v_lshlrev_b32_e32 v10, 2, v2
	v_lshl_add_u64 v[10:11], v[10:11], 2, s[28:29]
	global_load_dwordx3 v[22:24], v[26:27], off offset:4
	global_load_dwordx4 v[18:21], v[10:11], off
	v_lshlrev_b32_e32 v10, 2, v34
	v_ashrrev_i32_e32 v11, 31, v10
	v_lshlrev_b64 v[10:11], 2, v[10:11]
	s_waitcnt lgkmcnt(0)
	v_lshl_add_u64 v[12:13], s[34:35], 0, v[10:11]
	v_lshl_add_u64 v[10:11], s[28:29], 0, v[10:11]
	global_load_dwordx4 v[14:17], v[12:13], off
	v_cvt_f32_f16_e32 v29, v7
	global_load_dwordx4 v[10:13], v[10:11], off
	v_mov_b32_e32 v5, 0xff800000
	v_mov_b32_e32 v28, 0xff800000
	s_and_saveexec_b64 s[6:7], s[2:3]
	s_cbranch_execz .LBB2_45
	global_load_dword v25, v[26:27], off
	s_waitcnt vmcnt(0)
	v_add_f32_e32 v25, v14, v25
	v_add_f32_e32 v25, v25, v29
	v_mul_f32_e32 v26, 0x3e4ccccd, v25
	v_cmp_lt_f32_e32 vcc, 0, v25
	s_nop 1
	v_cndmask_b32_e32 v28, v26, v25, vcc

.LBB2_53:
	s_lshl_b32 s2, s41, 4
	s_mov_b32 s3, 0
	s_lshl_b32 s8, s41, 8
	s_lshl_b64 s[4:5], s[2:3], 10
	s_waitcnt lgkmcnt(0)
	s_add_u32 s6, s26, s4
	s_addc_u32 s7, s27, s5
	v_lshlrev_b32_e32 v46, 4, v68
	v_mov_b32_e32 v47, 0
	s_movk_i32 s2, 0x2000
	v_lshl_add_u64 v[14:15], s[6:7], 0, v[46:47]
	global_load_dwordx4 v[6:9], v46, s[6:7]
	v_add_co_u32_e32 v48, vcc, s2, v14
	s_movk_i32 s4, 0x1000
	s_nop 0
	v_addc_co_u32_e32 v49, vcc, 0, v15, vcc
	global_load_dwordx4 v[38:41], v[48:49], off offset:-4096
	global_load_dwordx4 v[26:29], v46, s[6:7] offset:1024
	v_add_co_u32_e32 v2, vcc, s4, v14
	s_andn2_b32 s43, s43, 63
	s_nop 0
	v_addc_co_u32_e32 v3, vcc, 0, v15, vcc
	global_load_dwordx4 v[42:45], v[2:3], off offset:1024
	global_load_dwordx4 v[34:37], v46, s[6:7] offset:2048
	global_load_dwordx4 v[30:33], v[2:3], off offset:2048
	global_load_dwordx4 v[22:25], v46, s[6:7] offset:3072
	global_load_dwordx4 v[18:21], v[2:3], off offset:3072
	v_or_b32_e32 v52, s43, v69
	v_ashrrev_i32_e32 v53, 31, v52
	v_lshlrev_b64 v[54:55], 2, v[52:53]
	v_lshl_add_u64 v[50:51], s[36:37], 0, v[54:55]
	global_load_dword v68, v[50:51], off
	global_load_dword v76, v[50:51], off offset:64
	v_lshl_add_u64 v[74:75], s[24:25], 0, v[54:55]
	v_mul_u32_u24_e32 v2, 0x410, v69
	v_and_b32_e32 v53, 48, v0
	global_load_dword v77, v[74:75], off
	global_load_dword v78, v[74:75], off offset:64
	v_add3_u32 v62, s8, v2, v53
	s_barrier
	ds_read_b128 v[2:5], v62
	ds_read_b128 v[10:13], v62 offset:64
	global_load_dwordx4 v[58:61], v[48:49], off
	v_mov_b32_e32 v70, 0x4100
	s_movk_i32 s2, 0x3000
	v_add_co_u32_e32 v66, vcc, s2, v14
	s_movk_i32 s2, 0x840
	s_nop 0
	v_addc_co_u32_e32 v67, vcc, 0, v15, vcc
	s_movk_i32 s5, 0x210
	global_load_dwordx4 v[14:17], v[66:67], off offset:3072
	s_waitcnt vmcnt(13) lgkmcnt(1)
	v_mfma_f32_16x16x32_f16 v[6:9], v[2:5], v[6:9], 0
	s_waitcnt vmcnt(12)
	v_mfma_f32_16x16x32_f16 v[38:41], v[2:5], v[38:41], 0
	s_waitcnt vmcnt(11) lgkmcnt(0)
	v_mfma_f32_16x16x32_f16 v[54:57], v[10:13], v[26:29], v[6:9]
	ds_read_b128 v[26:29], v62 offset:192
	s_nop 2
	ds_read_b128 v[6:9], v62 offset:128
	s_waitcnt vmcnt(10)
	v_mfma_f32_16x16x32_f16 v[38:41], v[10:13], v[42:45], v[38:41]
	global_load_dwordx4 v[42:45], v[48:49], off offset:1024
	global_load_dwordx4 v[62:65], v[48:49], off offset:2048
	s_waitcnt vmcnt(11) lgkmcnt(0)
	v_mfma_f32_16x16x32_f16 v[54:57], v[6:9], v[34:37], v[54:57]
	v_lshl_or_b32 v34, v1, 2, 1
	s_waitcnt vmcnt(10)
	v_mfma_f32_16x16x32_f16 v[36:39], v[6:9], v[30:33], v[38:41]
	v_lshl_add_u32 v30, v52, 1, v70
	global_load_dwordx4 v[70:73], v[48:49], off offset:3072
	v_mad_u32_u24 v35, v1, s2, v30
	v_mad_u32_u24 v52, v34, s5, v30
	global_load_dwordx4 v[30:33], v[66:67], off
	global_load_dword v79, v[50:51], off offset:128
	s_waitcnt vmcnt(12)
	v_mfma_f32_16x16x32_f16 v[54:57], v[26:29], v[22:25], v[54:57]
	s_lshl_b32 s2, s41, 3
	s_lshl_b64 s[2:3], s[2:3], 10
	s_add_u32 s2, s16, s2
	s_waitcnt vmcnt(11)
	v_mfma_f32_16x16x32_f16 v[36:39], v[26:29], v[18:21], v[36:39]
	global_load_dwordx4 v[22:25], v[66:67], off offset:1024
	global_load_dwordx4 v[18:21], v[66:67], off offset:2048
	s_nop 0
	global_load_dword v66, v[50:51], off offset:192
	global_load_dword v67, v[74:75], off offset:128
	s_nop 0
	global_load_dword v74, v[74:75], off offset:192
	s_waitcnt vmcnt(15)
	v_add_f32_e32 v40, v68, v54
	v_add_f32_e32 v41, v68, v55
	v_mul_f32_e32 v50, 0x3fb8aa3b, v40
	v_add_f32_e32 v48, v68, v56
	v_mul_f32_e32 v51, 0x3fb8aa3b, v41
	v_exp_f32_e32 v50, v50
	v_add_f32_e32 v49, v68, v57
	v_mul_f32_e32 v54, 0x3fb8aa3b, v48
	v_exp_f32_e32 v51, v51
	v_mul_f32_e32 v55, 0x3fb8aa3b, v49
	v_exp_f32_e32 v54, v54
	v_exp_f32_e32 v55, v55
	v_add_f32_e32 v50, -1.0, v50
	v_cmp_lt_f32_e32 vcc, 0, v40
	s_waitcnt vmcnt(14)
	v_add_f32_e32 v36, v76, v36
	v_add_f32_e32 v37, v76, v37
	v_cndmask_b32_e32 v40, v50, v40, vcc
	v_add_f32_e32 v50, -1.0, v51
	v_cmp_lt_f32_e32 vcc, 0, v41
	v_add_f32_e32 v51, -1.0, v54
	v_add_f32_e32 v54, -1.0, v55
	v_cndmask_b32_e32 v41, v50, v41, vcc
	v_cmp_lt_f32_e32 vcc, 0, v48
	s_waitcnt vmcnt(13)
	v_sub_f32_e32 v40, v40, v77
	v_sub_f32_e32 v41, v41, v77
	v_cndmask_b32_e32 v48, v51, v48, vcc
	v_cmp_lt_f32_e32 vcc, 0, v49
	v_sub_f32_e32 v48, v48, v77
	v_cvt_f16_f32_e32 v40, v40
	v_cndmask_b32_e32 v49, v54, v49, vcc
	v_cvt_f16_f32_e32 v41, v41
	v_sub_f32_e32 v49, v49, v77
	v_cvt_f16_f32_e32 v48, v48
	v_cvt_f16_f32_e32 v49, v49
	v_mul_f32_e32 v50, 0x3fb8aa3b, v36
	ds_write_b16 v35, v40
	v_exp_f32_e32 v40, v50
	ds_write_b16 v52, v41
	ds_write_b16 v52, v48 offset:528
	ds_write_b16 v52, v49 offset:1056
	v_mul_f32_e32 v41, 0x3fb8aa3b, v37
	v_exp_f32_e32 v41, v41
	v_add_f32_e32 v40, -1.0, v40
	v_cmp_lt_f32_e32 vcc, 0, v36
	v_add_f32_e32 v38, v76, v38
	s_waitcnt vmcnt(11)
	v_mfma_f32_16x16x32_f16 v[48:51], v[2:5], v[58:61], 0
	v_cndmask_b32_e32 v36, v40, v36, vcc
	v_add_f32_e32 v40, -1.0, v41
	v_cmp_lt_f32_e32 vcc, 0, v37
	v_sub_f32_e32 v36, v36, v78
	v_cvt_f16_f32_e32 v36, v36
	v_cndmask_b32_e32 v37, v40, v37, vcc
	v_mul_f32_e32 v40, 0x3fb8aa3b, v38
	v_sub_f32_e32 v37, v37, v78
	v_exp_f32_e32 v40, v40
	v_cvt_f16_f32_e32 v37, v37
	ds_write_b16 v35, v36 offset:32
	ds_write_b16 v52, v37 offset:32
	v_add_f32_e32 v36, -1.0, v40
	s_waitcnt vmcnt(9)
	v_mfma_f32_16x16x32_f16 v[40:43], v[10:13], v[42:45], v[48:51]
	v_cmp_lt_f32_e32 vcc, 0, v38
	v_add_f32_e32 v44, v76, v39
	s_addc_u32 s3, s17, s3
	v_cndmask_b32_e32 v54, v36, v38, vcc
	v_mul_f32_e32 v36, 0x3fb8aa3b, v44
	v_exp_f32_e32 v45, v36
	s_waitcnt vmcnt(8)
	v_mfma_f32_16x16x32_f16 v[36:39], v[6:9], v[62:65], v[40:43]
	v_cmp_lt_f32_e32 vcc, 0, v44
	s_waitcnt vmcnt(7)
	v_mfma_f32_16x16x32_f16 v[36:39], v[26:29], v[70:73], v[36:39]
	v_add_f32_e32 v41, -1.0, v45
	v_sub_f32_e32 v40, v54, v78
	v_cndmask_b32_e32 v41, v41, v44, vcc
	s_waitcnt vmcnt(6)
	v_mfma_f32_16x16x32_f16 v[2:5], v[2:5], v[30:33], 0
	s_waitcnt vmcnt(5)
	s_nop 1
	v_add_f32_e32 v36, v79, v36
	v_mul_f32_e32 v42, 0x3fb8aa3b, v36
	v_exp_f32_e32 v42, v42
	s_waitcnt vmcnt(4)
	v_mfma_f32_16x16x32_f16 v[2:5], v[10:13], v[22:25], v[2:5]
	v_cmp_lt_f32_e32 vcc, 0, v36
	v_cvt_f16_f32_e32 v40, v40
	v_add_f32_e32 v42, -1.0, v42
	v_sub_f32_e32 v41, v41, v78
	v_cndmask_b32_e32 v36, v42, v36, vcc
	v_cvt_f16_f32_e32 v41, v41
	s_waitcnt vmcnt(1)
	v_sub_f32_e32 v36, v36, v67
	v_mfma_f32_16x16x32_f16 v[2:5], v[6:9], v[18:21], v[2:5]
	v_cvt_f16_f32_e32 v36, v36
	v_add_f32_e32 v37, v79, v37
	v_mul_f32_e32 v42, 0x3fb8aa3b, v37
	v_add_f32_e32 v38, v79, v38
	v_exp_f32_e32 v42, v42
	ds_write_b16 v52, v40 offset:560
	ds_write_b16 v52, v41 offset:1088
	ds_write_b16 v35, v36 offset:64
	v_mul_f32_e32 v40, 0x3fb8aa3b, v38
	v_add_f32_e32 v30, v79, v39
	v_exp_f32_e32 v40, v40
	v_mul_f32_e32 v31, 0x3fb8aa3b, v30
	v_mfma_f32_16x16x32_f16 v[2:5], v[26:29], v[14:17], v[2:5]
	v_exp_f32_e32 v31, v31
	v_add_f32_e32 v36, -1.0, v42
	v_cmp_lt_f32_e32 vcc, 0, v37
	v_lshl_add_u64 v[18:19], s[2:3], 0, v[46:47]
	v_add_f32_e32 v11, -1.0, v31
	v_cndmask_b32_e32 v36, v36, v37, vcc
	v_add_f32_e32 v37, -1.0, v40
	v_cmp_lt_f32_e32 vcc, 0, v38
	v_add_f32_e32 v2, v66, v2
	v_sub_f32_e32 v36, v36, v67
	v_cndmask_b32_e32 v37, v37, v38, vcc
	v_cmp_lt_f32_e32 vcc, 0, v30
	v_mul_f32_e32 v7, 0x3fb8aa3b, v2
	v_cvt_f16_f32_e32 v36, v36
	v_sub_f32_e32 v10, v37, v67
	v_cndmask_b32_e32 v6, v11, v30, vcc
	v_exp_f32_e32 v7, v7
	v_cvt_f16_f32_e32 v10, v10
	v_sub_f32_e32 v6, v6, v67
	v_cvt_f16_f32_e32 v6, v6
	v_add_f32_e32 v3, v66, v3
	ds_write_b16 v52, v36 offset:64
	ds_write_b16 v52, v10 offset:592
	ds_write_b16 v52, v6 offset:1120
	v_add_f32_e32 v6, -1.0, v7
	v_mul_f32_e32 v7, 0x3fb8aa3b, v3
	v_exp_f32_e32 v7, v7
	v_cmp_lt_f32_e32 vcc, 0, v2
	v_add_f32_e32 v4, v66, v4
	v_add_f32_e32 v5, v66, v5
	v_cndmask_b32_e32 v2, v6, v2, vcc
	v_add_f32_e32 v6, -1.0, v7
	v_mul_f32_e32 v7, 0x3fb8aa3b, v4
	v_exp_f32_e32 v7, v7
	v_cmp_lt_f32_e32 vcc, 0, v3
	s_waitcnt vmcnt(0)
	v_sub_f32_e32 v2, v2, v74
	v_cvt_f16_f32_e32 v2, v2
	v_cndmask_b32_e32 v3, v6, v3, vcc
	v_add_f32_e32 v6, -1.0, v7
	v_mul_f32_e32 v7, 0x3fb8aa3b, v5
	v_exp_f32_e32 v7, v7
	v_cmp_lt_f32_e32 vcc, 0, v4
	v_sub_f32_e32 v3, v3, v74
	v_cvt_f16_f32_e32 v3, v3
	v_cndmask_b32_e32 v4, v6, v4, vcc
	v_add_f32_e32 v6, -1.0, v7
	v_cmp_lt_f32_e32 vcc, 0, v5
	v_sub_f32_e32 v4, v4, v74
	v_cvt_f16_f32_e32 v4, v4
	v_cndmask_b32_e32 v5, v6, v5, vcc
	v_sub_f32_e32 v5, v5, v74
	v_cvt_f16_f32_e32 v5, v5
	ds_write_b16 v35, v2 offset:96
	ds_write_b16 v52, v3 offset:96
	ds_write_b16 v52, v4 offset:624
	ds_write_b16 v52, v5 offset:1152
	s_waitcnt lgkmcnt(0)
	global_load_dwordx4 v[2:5], v46, s[2:3]
	global_load_dwordx4 v[6:9], v46, s[2:3] offset:1024
	global_load_dwordx4 v[10:13], v46, s[2:3] offset:2048
	global_load_dwordx4 v[14:17], v46, s[2:3] offset:3072
	v_add_co_u32_e32 v36, vcc, s4, v18
	v_mad_u32_u24 v35, v69, s5, v53
	s_nop 0
	v_addc_co_u32_e32 v37, vcc, 0, v19, vcc
	global_load_dwordx4 v[18:21], v[36:37], off
	global_load_dwordx4 v[22:25], v[36:37], off offset:1024
	global_load_dwordx4 v[26:29], v[36:37], off offset:2048
	global_load_dwordx4 v[30:33], v[36:37], off offset:3072
	s_barrier
	ds_read_b128 v[36:39], v35 offset:16640
	ds_read_b128 v[40:43], v35 offset:16704
	s_movk_i32 s2, 0x440
	s_waitcnt vmcnt(7) lgkmcnt(1)
	v_mfma_f32_16x16x32_f16 v[2:5], v[36:39], v[2:5], 0
	ds_read_b128 v[36:39], v35 offset:16768
	s_waitcnt vmcnt(6) lgkmcnt(1)
	v_mfma_f32_16x16x32_f16 v[2:5], v[40:43], v[6:9], v[2:5]
	ds_read_b128 v[6:9], v35 offset:16832
	s_waitcnt vmcnt(5) lgkmcnt(1)
	v_mfma_f32_16x16x32_f16 v[2:5], v[36:39], v[10:13], v[2:5]
	ds_read_b128 v[10:13], v35 offset:16896
	s_waitcnt vmcnt(4) lgkmcnt(1)
	v_mfma_f32_16x16x32_f16 v[2:5], v[6:9], v[14:17], v[2:5]
	ds_read_b128 v[6:9], v35 offset:16960
	s_waitcnt vmcnt(3) lgkmcnt(1)
	v_mfma_f32_16x16x32_f16 v[2:5], v[10:13], v[18:21], v[2:5]
	ds_read_b128 v[10:13], v35 offset:17024
	s_waitcnt vmcnt(2) lgkmcnt(1)
	v_mfma_f32_16x16x32_f16 v[2:5], v[6:9], v[22:25], v[2:5]
	ds_read_b128 v[6:9], v35 offset:17088
	s_waitcnt vmcnt(1) lgkmcnt(1)
	v_mfma_f32_16x16x32_f16 v[2:5], v[10:13], v[26:29], v[2:5]
	s_waitcnt vmcnt(0) lgkmcnt(0)
	v_mfma_f32_16x16x32_f16 v[2:5], v[6:9], v[30:33], v[2:5]
	v_lshlrev_b32_e32 v6, 2, v69
	v_lshl_or_b32 v7, s41, 6, v6
	v_mad_u32_u24 v1, v1, s2, v7
	s_movk_i32 s2, 0x110
	s_nop 3
	ds_write_b32 v1, v2
	v_mad_u32_u24 v1, v34, s2, v7
	v_lshlrev_b32_e32 v2, 4, v69
	ds_write2_b32 v1, v3, v4 offset1:68
	ds_write_b32 v1, v5 offset:544
	s_waitcnt lgkmcnt(0)
	global_load_dwordx4 v[8:11], v2, s[24:25] offset:1024
	global_load_dwordx4 v[12:15], v2, s[18:19]
	global_load_dwordx4 v[16:19], v2, s[14:15]
	v_lshrrev_b32_e32 v1, 4, v0
	v_mbcnt_lo_u32_b32 v3, -1, 0
	v_mad_u32_u24 v2, v1, s2, v2
	v_mbcnt_hi_u32_b32 v7, -1, v3
	s_barrier
	ds_read_b128 v[2:5], v2
	v_and_b32_e32 v20, 0x70, v7
	v_xor_b32_e32 v21, 8, v7
	v_add_u32_e32 v20, 16, v20
	v_cmp_lt_i32_e32 vcc, v21, v20
	v_xor_b32_e32 v22, 4, v7
	v_xor_b32_e32 v23, 2, v7
	v_cndmask_b32_e32 v21, v7, v21, vcc
	v_lshlrev_b32_e32 v21, 2, v21
	v_cmp_lt_i32_e32 vcc, v22, v20
	s_movk_i32 s2, 0x100
	s_waitcnt vmcnt(2) lgkmcnt(0)
	v_add_f32_e32 v9, v3, v9
	v_add_f32_e32 v8, v2, v8
	s_waitcnt vmcnt(1)
	v_mul_f32_e32 v13, v13, v9
	s_waitcnt vmcnt(0)
	v_mul_f32_e32 v9, v17, v9
	v_add_f32_e32 v10, v4, v10
	v_fmac_f32_e32 v13, v12, v8
	v_fmac_f32_e32 v9, v16, v8
	v_add_f32_e32 v11, v5, v11
	v_fmac_f32_e32 v13, v14, v10
	v_fmac_f32_e32 v9, v18, v10
	v_fmac_f32_e32 v13, v15, v11
	v_fmac_f32_e32 v9, v19, v11
	ds_bpermute_b32 v8, v21, v13
	ds_bpermute_b32 v10, v21, v9
	v_cndmask_b32_e32 v11, v7, v22, vcc
	v_lshlrev_b32_e32 v11, 2, v11
	v_cmp_lt_i32_e32 vcc, v23, v20
	s_waitcnt lgkmcnt(1)
	v_add_f32_e32 v8, v13, v8
	s_waitcnt lgkmcnt(0)
	v_add_f32_e32 v9, v9, v10
	ds_bpermute_b32 v10, v11, v8
	ds_bpermute_b32 v11, v11, v9
	v_cndmask_b32_e32 v12, v7, v23, vcc
	v_lshlrev_b32_e32 v12, 2, v12
	s_waitcnt lgkmcnt(1)
	v_add_f32_e32 v8, v8, v10
	s_waitcnt lgkmcnt(0)
	v_add_f32_e32 v9, v9, v11
	ds_bpermute_b32 v10, v12, v8
	ds_bpermute_b32 v11, v12, v9
	v_xor_b32_e32 v12, 1, v7
	v_cmp_lt_i32_e32 vcc, v12, v20
	s_nop 1
	v_cndmask_b32_e32 v12, v7, v12, vcc
	s_waitcnt lgkmcnt(1)
	v_add_f32_e32 v7, v8, v10
	s_waitcnt lgkmcnt(0)
	v_add_f32_e32 v8, v9, v11
	v_lshlrev_b32_e32 v10, 2, v12
	ds_bpermute_b32 v9, v10, v7
	ds_bpermute_b32 v10, v10, v8
	v_cmp_gt_u32_e32 vcc, s2, v0
	s_and_saveexec_b64 s[2:3], vcc
	s_cbranch_execz .LBB2_57
	v_lshlrev_b32_e32 v0, 2, v1
	ds_read_b32 v0, v0 offset:25152
	s_load_dwordx2 s[2:3], s[0:1], 0x50
	v_cmp_eq_u32_e32 vcc, 0, v69
	s_waitcnt lgkmcnt(0)
	v_add_u32_e32 v0, s33, v0
	v_ashrrev_i32_e32 v1, 31, v0
	s_and_saveexec_b64 s[4:5], vcc
	s_cbranch_execz .LBB2_56
	s_load_dwordx4 s[8:11], s[0:1], 0x58
	v_add_f32_e32 v7, v7, v9
	v_add_f32_e32 v12, v8, v10
	v_lshlrev_b64 v[8:9], 2, v[0:1]
	s_waitcnt lgkmcnt(0)
	v_lshl_add_u64 v[10:11], s[10:11], 0, v[8:9]
	v_lshl_add_u64 v[8:9], s[8:9], 0, v[8:9]
	global_store_dword v[8:9], v7, off
	global_store_dword v[10:11], v12, off

.LBB2_57:
	s_endpgm
	s_nop 0
	s_nop 0
	s_nop 0
	s_nop 0
	s_nop 0
	s_nop 0
	s_nop 0
	s_nop 0
	s_nop 0
	s_nop 0
	s_nop 0
	s_nop 0
	s_nop 0
	s_endpgm

.LBB3_2:
	s_or_b64 exec, exec, s[2:3]
	v_and_b32_e32 v33, 15, v0
	v_lshlrev_b32_e32 v34, 4, v33
	global_load_dwordx4 v[40:43], v34, s[8:9]
	global_load_dwordx4 v[44:47], v34, s[10:11] offset:1024
	global_load_dwordx4 v[2:5], v34, s[10:11] offset:2048
	s_load_dwordx2 s[10:11], s[0:1], 0x10
	s_load_dwordx2 s[8:9], s[0:1], 0x38
	v_and_b32_e32 v31, 63, v0
	s_and_b32 s13, s13, 0xffff
	s_waitcnt vmcnt(3)
	v_sub_u32_e32 v1, v1, v7
	v_cndmask_b32_e32 v37, 0, v1, vcc
	v_cmp_gt_i32_e32 vcc, 48, v37
	v_lshlrev_b32_e32 v0, 2, v33
	s_mov_b32 s15, 0x20000
	s_mov_b32 s14, 0x271000
	s_mov_b64 s[2:3], -1
	v_mbcnt_lo_u32_b32 v32, -1, 0
	s_cmp_eq_u64 vcc, exec
	v_cmp_gt_u32_e64 s[0:1], 16, v31
	v_lshlrev_b32_e32 v20, 1, v0
	v_lshlrev_b32_e32 v38, 3, v33
	s_cbranch_scc0 .LBB3_5
	s_and_b64 vcc, exec, s[2:3]
	s_cbranch_vccnz .LBB3_22

.LBB3_5:
	s_waitcnt vmcnt(0)
	v_pk_add_f32 v[0:1], v[40:41], v[44:45]
	v_pk_add_f32 v[18:19], v[42:43], v[46:47]
	v_mbcnt_hi_u32_b32 v8, -1, v32
	v_and_b32_e32 v13, 64, v8
	v_xor_b32_e32 v12, 16, v8
	v_add_u32_e32 v13, 64, v13
	v_cmp_lt_i32_e32 vcc, v12, v13
	v_mov_b32_e32 v9, 0
	v_mov_b32_e32 v21, v9
	v_cndmask_b32_e32 v12, v8, v12, vcc
	v_lshlrev_b32_e32 v34, 2, v12
	v_xor_b32_e32 v12, 32, v8
	v_cmp_lt_i32_e32 vcc, v12, v13
	v_lshlrev_b32_e32 v14, 2, v36
	s_movk_i32 s2, 0x100
	v_cndmask_b32_e32 v12, v8, v12, vcc
	v_lshlrev_b32_e32 v8, 2, v8
	v_lshl_add_u64 v[10:11], s[16:17], 0, v[20:21]
	s_mov_b32 s23, 0
	v_lshlrev_b32_e32 v35, 2, v12
	s_waitcnt lgkmcnt(0)
	v_lshl_add_u64 v[12:13], s[8:9], 0, v[20:21]
	v_and_or_b32 v21, v8, s2, v14
	s_branch .LBB3_7

.LBB3_22:
	v_add_u32_e32 v8, v7, v33
	v_cmp_lt_i32_e64 s[0:1], v33, v37
	v_or_b32_e32 v24, 16, v33
	v_or_b32_e32 v21, 32, v33
	v_ashrrev_i32_e32 v9, 31, v8
	v_cmp_lt_i32_e64 s[2:3], v24, v37
	v_cmp_lt_i32_e64 s[4:5], v21, v37
	v_lshl_add_u64 v[26:27], v[8:9], 4, s[6:7]
	v_mov_b32_e32 v15, v6
	v_mov_b32_e32 v17, 0
	v_mov_b32_e32 v10, v6
	v_mov_b32_e32 v13, 0
	v_mov_b32_e32 v9, 0
	s_mov_b64 s[16:17], exec
	s_mov_b64 exec, s[0:1]
	s_cbranch_execz .Ll2_csr1
	global_load_dwordx4 v[14:17], v[26:27], off nt
.Ll2_csr1:
	s_mov_b64 exec, s[2:3]
	s_cbranch_execz .Ll2_csr2
	global_load_dwordx4 v[10:13], v[26:27], off offset:256 nt
.Ll2_csr2:
	s_mov_b64 exec, s[4:5]
	s_cbranch_execz .Ll2_csr3
	global_load_dwordx4 v[6:9], v[26:27], off offset:512 nt
.Ll2_csr3:
	s_mov_b64 exec, s[16:17]
	s_waitcnt vmcnt(0)
	v_pk_add_f32 v[0:1], v[40:41], v[44:45]
	v_pk_add_f32 v[18:19], v[42:43], v[46:47]
	v_cndmask_b32_e64 v15, v15, v14, s[0:1]
	v_or_b32_e32 v16, 16, v33
	v_mov_b32_e32 v11, 0
	v_lshl_add_u64 v[26:27], v[10:11], 2, s[18:19]
	v_mov_b32_e32 v7, v11
	v_lshlrev_b64 v[22:23], 2, v[22:23]
	s_waitcnt lgkmcnt(0)
	v_lshl_add_u64 v[28:29], v[6:7], 2, s[18:19]
	global_load_dword v14, v[26:27], off
	global_load_dword v24, v[28:29], off
	v_lshl_add_u64 v[26:27], s[10:11], 0, v[22:23]
	v_lshl_add_u64 v[22:23], s[18:19], 0, v[22:23]
	global_load_dword v8, v[26:27], off
	global_load_dword v12, v[22:23], off
	v_mov_b32_e32 v7, 0xff800000
	v_mov_b32_e32 v11, 0xff800000
	s_and_saveexec_b64 s[6:7], s[0:1]
	s_cbranch_execnz .LBB3_54
	s_or_b64 exec, exec, s[6:7]
	s_and_saveexec_b64 s[6:7], s[2:3]
	s_cbranch_execnz .LBB3_55

.LBB3_32:
	s_or_b64 exec, exec, s[6:7]
	v_add_f32_e32 v17, 0, v17
	v_add_f32_e32 v13, v17, v13
	v_add_f32_e32 v9, v13, v9
	v_mov_b32_e32 v13, v9
	v_cvt_f32_i32_e32 v17, v37
	v_max_f32_e32 v22, v11, v11
	v_mov_b32_dpp v13, v13 quad_perm:[1,0,3,2] row_mask:0xf bank_mask:0xf
	v_add_f32_e32 v9, v9, v13
	v_mov_b32_e32 v13, v9
	v_max_f32_e32 v22, 0xff800000, v22
	v_max3_f32 v22, v22, v7, v14
	v_mov_b32_dpp v13, v13 quad_perm:[2,3,0,1] row_mask:0xf bank_mask:0xf
	v_add_f32_e32 v9, v9, v13
	v_mov_b32_e32 v13, v9
	s_nop 1
	v_mov_b32_dpp v13, v13 row_half_mirror row_mask:0xf bank_mask:0xf
	v_add_f32_e32 v9, v9, v13
	v_mov_b32_e32 v13, v9
	s_nop 1
	v_mov_b32_dpp v13, v13 row_mirror row_mask:0xf bank_mask:0xf
	s_waitcnt vmcnt(0)
	v_pk_add_f32 v[8:9], v[8:9], v[12:13]
	v_max_f32_e32 v12, 1.0, v17
	v_div_scale_f32 v13, s[6:7], v12, v12, v9
	v_rcp_f32_e32 v17, v13
	s_movk_i32 s7, 0x180
	s_mov_b32 s6, 0
	v_fma_f32 v23, -v13, v17, 1.0
	v_fmac_f32_e32 v17, v23, v17
	v_div_scale_f32 v23, vcc, v9, v12, v9
	v_mul_f32_e32 v24, v23, v17
	v_fma_f32 v25, -v13, v24, v23
	v_fmac_f32_e32 v24, v25, v17
	v_fma_f32 v13, -v13, v24, v23
	v_div_fmas_f32 v13, v13, v17, v24
	v_div_fixup_f32 v9, v13, v12, v9
	v_add_f32_e32 v8, v8, v9
	v_mul_f32_e32 v9, 0x3e4ccccd, v8
	v_cmp_lt_f32_e32 vcc, 0, v8
	s_nop 1
	v_cndmask_b32_e32 v8, v9, v8, vcc
	v_mov_b32_e32 v9, v22
	v_cmp_eq_u32_e32 vcc, v33, v37
	s_nop 0
	v_mov_b32_dpp v9, v9 quad_perm:[1,0,3,2] row_mask:0xf bank_mask:0xf
	v_max_f32_e32 v9, v9, v9
	v_max_f32_e32 v9, v22, v9
	v_mov_b32_e32 v12, v9
	s_nop 1
	v_mov_b32_dpp v12, v12 quad_perm:[2,3,0,1] row_mask:0xf bank_mask:0xf
	v_max_f32_e32 v12, v12, v12
	v_max_f32_e32 v9, v9, v12
	v_mov_b32_e32 v12, v9
	s_nop 1
	v_mov_b32_dpp v12, v12 row_half_mirror row_mask:0xf bank_mask:0xf
	v_max_f32_e32 v12, v12, v12
	v_max_f32_e32 v9, v9, v12
	v_mov_b32_e32 v12, v9
	s_nop 1
	v_mov_b32_dpp v12, v12 row_mirror row_mask:0xf bank_mask:0xf
	v_max3_f32 v9, v9, v12, v8
	v_sub_f32_e32 v11, v11, v9
	v_mul_f32_e32 v11, 0x3fb8aa3b, v11
	v_sub_f32_e32 v7, v7, v9
	v_exp_f32_e32 v11, v11
	v_mul_f32_e32 v7, 0x3fb8aa3b, v7
	v_sub_f32_e32 v13, v14, v9
	v_exp_f32_e32 v7, v7
	v_mul_f32_e32 v13, 0x3fb8aa3b, v13
	v_exp_f32_e32 v13, v13
	v_add_f32_e32 v12, 0, v11
	v_cndmask_b32_e64 v12, 0, v12, s[0:1]
	v_cndmask_b32_e64 v14, 0, v7, s[2:3]
	v_add_f32_e32 v12, v12, v14
	v_cndmask_b32_e64 v14, 0, v13, s[4:5]
	v_add_f32_e32 v12, v12, v14
	v_sub_f32_e32 v8, v8, v9
	v_mov_b32_e32 v9, v12
	v_mul_f32_e32 v8, 0x3fb8aa3b, v8
	v_exp_f32_e32 v8, v8
	v_mov_b32_dpp v9, v9 quad_perm:[1,0,3,2] row_mask:0xf bank_mask:0xf
	v_add_f32_e32 v9, v12, v9
	v_mov_b32_e32 v12, v9
	s_nop 1
	v_mov_b32_dpp v12, v12 quad_perm:[2,3,0,1] row_mask:0xf bank_mask:0xf
	v_add_f32_e32 v9, v9, v12
	v_mov_b32_e32 v12, v9
	s_nop 1
	v_mov_b32_dpp v12, v12 row_half_mirror row_mask:0xf bank_mask:0xf
	v_add_f32_e32 v9, v9, v12
	v_mov_b32_e32 v12, v9
	s_nop 1
	v_mov_b32_dpp v12, v12 row_mirror row_mask:0xf bank_mask:0xf
	v_add_f32_e32 v9, v9, v12
	v_add_f32_e32 v9, v8, v9
	v_add_f32_e32 v9, 0x24e69595, v9
	v_rcp_f32_e32 v12, v9
	v_or_b32_e32 v9, s22, v36
	v_mul_lo_u32 v9, v9, s7
	v_or_b32_e32 v17, v9, v38
	v_mul_f32_e32 v22, v8, v12
	v_mul_f32_e32 v8, v12, v11
	v_cndmask_b32_e32 v9, 0, v22, vcc
	v_cmp_eq_u32_e32 vcc, v16, v37
	v_cndmask_b32_e64 v14, v9, v8, s[0:1]
	v_mul_f32_e32 v7, v12, v7
	v_cndmask_b32_e32 v8, 0, v22, vcc
	v_cndmask_b32_e64 v8, v8, v7, s[2:3]
	v_mov_b32_e32 v9, v10
	v_cmp_eq_u32_e32 vcc, v21, v37
	ds_write2_b64 v17, v[14:15], v[8:9] offset1:16
	v_mul_f32_e32 v7, v12, v13
	v_cndmask_b32_e32 v8, 0, v22, vcc
	v_readlane_b32 s0, v37, 0
	v_cndmask_b32_e64 v8, v8, v7, s[4:5]
	v_mov_b32_e32 v9, v6
	s_mul_i32 s7, s22, 0x180
	s_add_i32 s2, s0, 1
	ds_write_b64 v17, v[8:9] offset:256
	s_setprio 3
	v_readlane_b32 s1, v37, 16
	v_readlane_b32 s2, v37, 32
	v_readlane_b32 s3, v37, 48
	v_or_b32_e32 v6, s22, v36
	v_mul_u32_u24_e32 v6, 0x180, v6
	v_mov_b32_e32 v48, 0
	v_mov_b32_e32 v49, 0
	s_max_i32 s0, s0, s1
	s_max_i32 s2, s2, s3
	s_max_i32 s0, s0, s2
	s_add_i32 s0, s0, 4
	s_and_b32 s0, s0, -4
	s_mov_b32 s1, 0
	v_mov_b32_e32 v50, 0
	v_mov_b32_e32 v51, 0
	ds_read2_b64 v[8:11], v6 offset0:0 offset1:1
	ds_read2_b64 v[12:15], v6 offset0:2 offset1:3
	s_waitcnt lgkmcnt(0)
	v_lshl_or_b32 v9, v9, 7, v38
	v_lshl_or_b32 v11, v11, 7, v38
	v_lshl_or_b32 v13, v13, 7, v38
	v_lshl_or_b32 v15, v15, 7, v38
	buffer_load_dwordx2 v[20:21], v9, s[12:15], 0 offen
	buffer_load_dwordx2 v[22:23], v11, s[12:15], 0 offen
	buffer_load_dwordx2 v[24:25], v13, s[12:15], 0 offen
	buffer_load_dwordx2 v[26:27], v15, s[12:15], 0 offen
.Ll2g_loop:
	s_add_i32 s1, s1, 4
	s_cmp_ge_i32 s1, s0
	s_cbranch_scc1 .Ll2g_lastA
	ds_read2_b64 v[28:31], v6 offset0:4 offset1:5
	ds_read2_b64 v[32:35], v6 offset0:6 offset1:7
	s_waitcnt lgkmcnt(0)
	v_lshl_or_b32 v29, v29, 7, v38
	v_lshl_or_b32 v31, v31, 7, v38
	v_lshl_or_b32 v33, v33, 7, v38
	v_lshl_or_b32 v35, v35, 7, v38
	buffer_load_dwordx2 v[40:41], v29, s[12:15], 0 offen
	buffer_load_dwordx2 v[42:43], v31, s[12:15], 0 offen
	buffer_load_dwordx2 v[44:45], v33, s[12:15], 0 offen
	buffer_load_dwordx2 v[46:47], v35, s[12:15], 0 offen
	s_waitcnt vmcnt(4)
	v_cvt_f32_f16_sdwa v53, v20 dst_sel:DWORD dst_unused:UNUSED_PAD src0_sel:WORD_1
	v_cvt_f32_f16_e32 v52, v20
	v_cvt_f32_f16_sdwa v55, v21 dst_sel:DWORD dst_unused:UNUSED_PAD src0_sel:WORD_1
	v_cvt_f32_f16_e32 v54, v21
	v_pk_fma_f32 v[48:49], v[8:9], v[52:53], v[48:49] op_sel_hi:[0,1,1]
	v_pk_fma_f32 v[50:51], v[8:9], v[54:55], v[50:51] op_sel_hi:[0,1,1]
	v_cvt_f32_f16_sdwa v57, v22 dst_sel:DWORD dst_unused:UNUSED_PAD src0_sel:WORD_1
	v_cvt_f32_f16_e32 v56, v22
	v_cvt_f32_f16_sdwa v59, v23 dst_sel:DWORD dst_unused:UNUSED_PAD src0_sel:WORD_1
	v_cvt_f32_f16_e32 v58, v23
	v_pk_fma_f32 v[48:49], v[10:11], v[56:57], v[48:49] op_sel_hi:[0,1,1]
	v_pk_fma_f32 v[50:51], v[10:11], v[58:59], v[50:51] op_sel_hi:[0,1,1]
	v_cvt_f32_f16_sdwa v53, v24 dst_sel:DWORD dst_unused:UNUSED_PAD src0_sel:WORD_1
	v_cvt_f32_f16_e32 v52, v24
	v_cvt_f32_f16_sdwa v55, v25 dst_sel:DWORD dst_unused:UNUSED_PAD src0_sel:WORD_1
	v_cvt_f32_f16_e32 v54, v25
	v_pk_fma_f32 v[48:49], v[12:13], v[52:53], v[48:49] op_sel_hi:[0,1,1]
	v_pk_fma_f32 v[50:51], v[12:13], v[54:55], v[50:51] op_sel_hi:[0,1,1]
	v_cvt_f32_f16_sdwa v57, v26 dst_sel:DWORD dst_unused:UNUSED_PAD src0_sel:WORD_1
	v_cvt_f32_f16_e32 v56, v26
	v_cvt_f32_f16_sdwa v59, v27 dst_sel:DWORD dst_unused:UNUSED_PAD src0_sel:WORD_1
	v_cvt_f32_f16_e32 v58, v27
	v_pk_fma_f32 v[48:49], v[14:15], v[56:57], v[48:49] op_sel_hi:[0,1,1]
	v_pk_fma_f32 v[50:51], v[14:15], v[58:59], v[50:51] op_sel_hi:[0,1,1]
	s_add_i32 s1, s1, 4
	s_cmp_ge_i32 s1, s0
	s_cbranch_scc1 .Ll2g_lastB
	ds_read2_b64 v[8:11], v6 offset0:8 offset1:9
	ds_read2_b64 v[12:15], v6 offset0:10 offset1:11
	v_add_u32_e32 v6, 64, v6
	s_waitcnt lgkmcnt(0)
	v_lshl_or_b32 v9, v9, 7, v38
	v_lshl_or_b32 v11, v11, 7, v38
	v_lshl_or_b32 v13, v13, 7, v38
	v_lshl_or_b32 v15, v15, 7, v38
	buffer_load_dwordx2 v[20:21], v9, s[12:15], 0 offen
	buffer_load_dwordx2 v[22:23], v11, s[12:15], 0 offen
	buffer_load_dwordx2 v[24:25], v13, s[12:15], 0 offen
	buffer_load_dwordx2 v[26:27], v15, s[12:15], 0 offen
	s_waitcnt vmcnt(4)
	v_cvt_f32_f16_sdwa v53, v40 dst_sel:DWORD dst_unused:UNUSED_PAD src0_sel:WORD_1
	v_cvt_f32_f16_e32 v52, v40
	v_cvt_f32_f16_sdwa v55, v41 dst_sel:DWORD dst_unused:UNUSED_PAD src0_sel:WORD_1
	v_cvt_f32_f16_e32 v54, v41
	v_pk_fma_f32 v[48:49], v[28:29], v[52:53], v[48:49] op_sel_hi:[0,1,1]
	v_pk_fma_f32 v[50:51], v[28:29], v[54:55], v[50:51] op_sel_hi:[0,1,1]
	v_cvt_f32_f16_sdwa v57, v42 dst_sel:DWORD dst_unused:UNUSED_PAD src0_sel:WORD_1
	v_cvt_f32_f16_e32 v56, v42
	v_cvt_f32_f16_sdwa v59, v43 dst_sel:DWORD dst_unused:UNUSED_PAD src0_sel:WORD_1
	v_cvt_f32_f16_e32 v58, v43
	v_pk_fma_f32 v[48:49], v[30:31], v[56:57], v[48:49] op_sel_hi:[0,1,1]
	v_pk_fma_f32 v[50:51], v[30:31], v[58:59], v[50:51] op_sel_hi:[0,1,1]
	v_cvt_f32_f16_sdwa v53, v44 dst_sel:DWORD dst_unused:UNUSED_PAD src0_sel:WORD_1
	v_cvt_f32_f16_e32 v52, v44
	v_cvt_f32_f16_sdwa v55, v45 dst_sel:DWORD dst_unused:UNUSED_PAD src0_sel:WORD_1
	v_cvt_f32_f16_e32 v54, v45
	v_pk_fma_f32 v[48:49], v[32:33], v[52:53], v[48:49] op_sel_hi:[0,1,1]
	v_pk_fma_f32 v[50:51], v[32:33], v[54:55], v[50:51] op_sel_hi:[0,1,1]
	v_cvt_f32_f16_sdwa v57, v46 dst_sel:DWORD dst_unused:UNUSED_PAD src0_sel:WORD_1
	v_cvt_f32_f16_e32 v56, v46
	v_cvt_f32_f16_sdwa v59, v47 dst_sel:DWORD dst_unused:UNUSED_PAD src0_sel:WORD_1
	v_cvt_f32_f16_e32 v58, v47
	v_pk_fma_f32 v[48:49], v[34:35], v[56:57], v[48:49] op_sel_hi:[0,1,1]
	v_pk_fma_f32 v[50:51], v[34:35], v[58:59], v[50:51] op_sel_hi:[0,1,1]
	s_branch .Ll2g_loop
.Ll2g_lastA:
	s_waitcnt vmcnt(0)
	v_cvt_f32_f16_sdwa v53, v20 dst_sel:DWORD dst_unused:UNUSED_PAD src0_sel:WORD_1
	v_cvt_f32_f16_e32 v52, v20
	v_cvt_f32_f16_sdwa v55, v21 dst_sel:DWORD dst_unused:UNUSED_PAD src0_sel:WORD_1
	v_cvt_f32_f16_e32 v54, v21
	v_pk_fma_f32 v[48:49], v[8:9], v[52:53], v[48:49] op_sel_hi:[0,1,1]
	v_pk_fma_f32 v[50:51], v[8:9], v[54:55], v[50:51] op_sel_hi:[0,1,1]
	v_cvt_f32_f16_sdwa v57, v22 dst_sel:DWORD dst_unused:UNUSED_PAD src0_sel:WORD_1
	v_cvt_f32_f16_e32 v56, v22
	v_cvt_f32_f16_sdwa v59, v23 dst_sel:DWORD dst_unused:UNUSED_PAD src0_sel:WORD_1
	v_cvt_f32_f16_e32 v58, v23
	v_pk_fma_f32 v[48:49], v[10:11], v[56:57], v[48:49] op_sel_hi:[0,1,1]
	v_pk_fma_f32 v[50:51], v[10:11], v[58:59], v[50:51] op_sel_hi:[0,1,1]
	v_cvt_f32_f16_sdwa v53, v24 dst_sel:DWORD dst_unused:UNUSED_PAD src0_sel:WORD_1
	v_cvt_f32_f16_e32 v52, v24
	v_cvt_f32_f16_sdwa v55, v25 dst_sel:DWORD dst_unused:UNUSED_PAD src0_sel:WORD_1
	v_cvt_f32_f16_e32 v54, v25
	v_pk_fma_f32 v[48:49], v[12:13], v[52:53], v[48:49] op_sel_hi:[0,1,1]
	v_pk_fma_f32 v[50:51], v[12:13], v[54:55], v[50:51] op_sel_hi:[0,1,1]
	v_cvt_f32_f16_sdwa v57, v26 dst_sel:DWORD dst_unused:UNUSED_PAD src0_sel:WORD_1
	v_cvt_f32_f16_e32 v56, v26
	v_cvt_f32_f16_sdwa v59, v27 dst_sel:DWORD dst_unused:UNUSED_PAD src0_sel:WORD_1
	v_cvt_f32_f16_e32 v58, v27
	v_pk_fma_f32 v[48:49], v[14:15], v[56:57], v[48:49] op_sel_hi:[0,1,1]
	v_pk_fma_f32 v[50:51], v[14:15], v[58:59], v[50:51] op_sel_hi:[0,1,1]
	s_branch .Ll2g_done
.Ll2g_lastB:
	s_waitcnt vmcnt(0)
	v_cvt_f32_f16_sdwa v53, v40 dst_sel:DWORD dst_unused:UNUSED_PAD src0_sel:WORD_1
	v_cvt_f32_f16_e32 v52, v40
	v_cvt_f32_f16_sdwa v55, v41 dst_sel:DWORD dst_unused:UNUSED_PAD src0_sel:WORD_1
	v_cvt_f32_f16_e32 v54, v41
	v_pk_fma_f32 v[48:49], v[28:29], v[52:53], v[48:49] op_sel_hi:[0,1,1]
	v_pk_fma_f32 v[50:51], v[28:29], v[54:55], v[50:51] op_sel_hi:[0,1,1]
	v_cvt_f32_f16_sdwa v57, v42 dst_sel:DWORD dst_unused:UNUSED_PAD src0_sel:WORD_1
	v_cvt_f32_f16_e32 v56, v42
	v_cvt_f32_f16_sdwa v59, v43 dst_sel:DWORD dst_unused:UNUSED_PAD src0_sel:WORD_1
	v_cvt_f32_f16_e32 v58, v43
	v_pk_fma_f32 v[48:49], v[30:31], v[56:57], v[48:49] op_sel_hi:[0,1,1]
	v_pk_fma_f32 v[50:51], v[30:31], v[58:59], v[50:51] op_sel_hi:[0,1,1]
	v_cvt_f32_f16_sdwa v53, v44 dst_sel:DWORD dst_unused:UNUSED_PAD src0_sel:WORD_1
	v_cvt_f32_f16_e32 v52, v44
	v_cvt_f32_f16_sdwa v55, v45 dst_sel:DWORD dst_unused:UNUSED_PAD src0_sel:WORD_1
	v_cvt_f32_f16_e32 v54, v45
	v_pk_fma_f32 v[48:49], v[32:33], v[52:53], v[48:49] op_sel_hi:[0,1,1]
	v_pk_fma_f32 v[50:51], v[32:33], v[54:55], v[50:51] op_sel_hi:[0,1,1]
	v_cvt_f32_f16_sdwa v57, v46 dst_sel:DWORD dst_unused:UNUSED_PAD src0_sel:WORD_1
	v_cvt_f32_f16_e32 v56, v46
	v_cvt_f32_f16_sdwa v59, v47 dst_sel:DWORD dst_unused:UNUSED_PAD src0_sel:WORD_1
	v_cvt_f32_f16_e32 v58, v47
	v_pk_fma_f32 v[48:49], v[34:35], v[56:57], v[48:49] op_sel_hi:[0,1,1]
	v_pk_fma_f32 v[50:51], v[34:35], v[58:59], v[50:51] op_sel_hi:[0,1,1]
.Ll2g_done:
	s_setprio 0
	v_pk_add_f32 v[48:49], v[48:49], v[0:1]
	v_pk_add_f32 v[50:51], v[50:51], v[18:19]
	v_add_u32_e32 v10, s21, v36
	v_mul_f32_e32 v52, 0x3fb8aa3b, v48
	v_mul_f32_e32 v53, 0x3fb8aa3b, v49
	v_mul_f32_e32 v54, 0x3fb8aa3b, v50
	v_mul_f32_e32 v55, 0x3fb8aa3b, v51
	v_exp_f32_e32 v52, v52
	v_exp_f32_e32 v53, v53
	v_exp_f32_e32 v54, v54
	v_exp_f32_e32 v55, v55
	v_cmp_lt_f32_e64 s[0:1], 0, v48
	v_cmp_lt_f32_e64 s[2:3], 0, v49
	v_cmp_lt_f32_e64 s[4:5], 0, v50
	v_cmp_lt_f32_e64 s[6:7], 0, v51
	v_add_f32_e32 v52, -1.0, v52
	v_add_f32_e32 v53, -1.0, v53
	v_add_f32_e32 v54, -1.0, v54
	v_add_f32_e32 v55, -1.0, v55
	v_cndmask_b32_e64 v48, v52, v48, s[0:1]
	v_cndmask_b32_e64 v49, v53, v49, s[2:3]
	v_cndmask_b32_e64 v50, v54, v50, s[4:5]
	v_cndmask_b32_e64 v51, v55, v51, s[6:7]
	v_cmp_gt_i32_e32 vcc, s20, v10
	v_pk_add_f32 v[48:49], v[48:49], v[2:3] neg_lo:[0,1] neg_hi:[0,1]
	v_pk_add_f32 v[50:51], v[50:51], v[4:5] neg_lo:[0,1] neg_hi:[0,1]
	v_lshl_or_b32 v10, v10, 7, v38
	v_cvt_pk_f16_f32 v8, v48, v49
	v_cvt_pk_f16_f32 v9, v50, v51
	s_and_saveexec_b64 s[0:1], vcc
	global_store_dwordx2 v10, v[8:9], s[8:9]
	s_endpgm

.LBB3_55:
	s_waitcnt vmcnt(1)
	v_add_f32_e32 v7, v8, v14
	v_add_f32_e32 v7, v13, v7
	v_mul_f32_e32 v14, 0x3e4ccccd, v7
	v_cmp_lt_f32_e32 vcc, 0, v7
	s_nop 1
	v_cndmask_b32_e32 v7, v14, v7, vcc
	s_or_b64 exec, exec, s[6:7]
	v_mov_b32_e32 v14, 0xff800000
	s_and_saveexec_b64 s[6:7], s[4:5]
	s_cbranch_execnz .LBB3_31
	s_branch .LBB3_32
	s_nop 0
	s_nop 0
	s_nop 0
	s_nop 0
	s_nop 0
	s_nop 0
	s_nop 0
	s_nop 0
	s_nop 0
	s_nop 0
	s_nop 0
	s_nop 0
	s_nop 0
	s_nop 0
	s_nop 0
	s_nop 0
	s_nop 0
	s_nop 0
	s_nop 0
	s_nop 0
	s_nop 0
	s_nop 0
	s_nop 0
	s_nop 0
	s_nop 0
	s_nop 0
	s_nop 0
	s_nop 0
	s_nop 0
	s_nop 0
	s_nop 0
	s_nop 0
	s_nop 0
	s_nop 0
	s_nop 0
	s_nop 0
	s_nop 0
	s_nop 0
	s_nop 0
	s_nop 0
	s_nop 0
	s_nop 0
	s_nop 0
	s_nop 0
	s_nop 0
	s_nop 0
	s_nop 0
	s_nop 0
	s_nop 0
	s_nop 0
	s_nop 0
	s_nop 0
	s_nop 0
	s_nop 0
	s_endpgm
